# plus attention tile loops with one signed-slope bias block and the edge mask out of line; last three q/k/v epilogue stores deferred into the next unit's peeled iteration with exactly raised counted wa
# speedup vs baseline: 1.0016x; 1.0016x over previous
.LBB0_132:
	s_add_u32 s42, s75, 0xf100000
	s_addc_u32 s43, s74, 0
	s_add_u32 s44, s75, 0x2d100000
	s_addc_u32 s45, s74, 0
	s_add_u32 s46, s75, 0x35100000
	s_addc_u32 s47, s74, 0
	s_lshl_b32 s22, s52, 11
	s_lshl_b64 s[12:13], s[22:23], 2
	s_add_u32 s48, s10, s12
	s_addc_u32 s49, s9, s13
	s_add_u32 s50, s75, 0x15100000
	s_addc_u32 s51, s74, 0
	s_add_u32 s52, s75, 0x1b100000
	s_addc_u32 s53, s74, 0
	s_add_u32 s54, s75, 0x21100000
	s_addc_u32 s55, s74, 0
	s_and_b32 s10, s6, 3
	s_add_i32 m0, s93, 0x18000
	v_lshl_add_u64 v[6:7], v[6:7], 0, s[88:89]
	s_lshl_b32 s14, s8, 13
	s_lshl_b32 s16, s10, 12
	s_waitcnt vmcnt(2)
	s_barrier
	global_load_lds_dwordx4 v[6:7], off
	v_lshl_add_u64 v[4:5], v[4:5], 0, s[88:89]
	s_add_i32 m0, s93, 0x1a000
	s_add_i32 s9, s93, 0x8000
	s_add_i32 s97, s93, 0xa000
	global_load_lds_dwordx4 v[4:5], off
	v_lshl_add_u64 v[0:1], v[0:1], 0, s[88:89]
	s_mov_b32 m0, s9
	s_add_u32 s12, s0, 0x8080
	global_load_lds_dwordx4 v[0:1], off
	v_lshl_add_u64 v[0:1], v[2:3], 0, s[88:89]
	s_mov_b32 m0, s97
	s_addc_u32 s13, s1, 0
	global_load_lds_dwordx4 v[0:1], off
	s_add_i32 m0, s93, 0x1c000
	v_lshl_add_u64 v[0:1], s[12:13], 0, v[166:167]
	global_load_lds_dwordx4 v[0:1], off
	v_lshl_add_u64 v[0:1], s[12:13], 0, v[162:163]
	s_add_i32 m0, s93, 0x1e000
	v_lshlrev_b32_e32 v5, 2, v8
	global_load_lds_dwordx4 v[0:1], off
	v_bfe_u32 v1, v8, 4, 2
	v_and_b32_e32 v0, 15, v8
	v_lshlrev_b32_e32 v4, 4, v1
	v_lshl_or_b32 v2, s8, 6, v0
	v_lshl_or_b32 v4, v0, 6, v4
	v_lshlrev_b32_e32 v0, 3, v0
	v_lshlrev_b32_e32 v3, 3, v1
	v_and_b32_e32 v5, 32, v5
	v_lshl_or_b32 v0, v1, 7, v0
	v_and_b32_e32 v1, 1, v8
	s_sext_i32_i16 s6, s36
	v_bitop3_b32 v6, v4, s14, v5 bitop3:0xde
	v_bitop3_b32 v182, v4, s16, v5 bitop3:0xde
	v_cmp_eq_u32_e64 s[36:37], 0, v1
	v_lshlrev_b32_e32 v4, 5, v1
	v_sub_u32_e32 v183, v2, v1
	v_lshlrev_b32_e32 v1, 13, v13
	v_and_b32_e32 v1, 0xffffc000, v1
	v_lshl_add_u32 v1, v12, 10, v1
	v_and_b32_e32 v2, 1, v13
	v_lshl_or_b32 v1, v2, 6, v1
	s_cmpk_lt_u32 s7, 0x100
	v_lshl_add_u32 v170, v14, 1, v1
	v_lshlrev_b32_e32 v1, 13, v9
	s_cselect_b64 s[56:57], -1, 0
	s_lshl_b32 s7, s8, 2
	v_and_b32_e32 v1, 0xffffc000, v1
	s_waitcnt vmcnt(6)
	s_or_b32 s8, s7, s10
	s_lshl_b32 s7, s10, 6
	v_lshl_add_u32 v1, v10, 10, v1
	v_and_b32_e32 v2, 1, v9
	s_add_u32 s58, s48, 0x1000
	v_lshl_or_b32 v1, v2, 6, v1
	s_mov_b32 s22, 0
	s_addc_u32 s59, s49, 0
	v_lshl_or_b32 v184, s10, 5, v3
	v_or3_b32 v185, s7, v4, v3
	v_mov_b32_e32 v171, v49
	v_lshl_add_u32 v172, v11, 1, v1
	v_mov_b32_e32 v173, v49
	v_add_u32_e32 v186, 0, v6
	v_lshlrev_b32_e32 v187, 1, v0
	s_barrier
	v_mov_b32_e32 v32, 0
	v_mov_b32_e32 v33, 0
	v_mov_b32_e32 v34, 0
	v_mov_b32_e32 v35, 0
	v_mov_b32_e32 v36, 0
	v_mov_b32_e32 v37, 0
	v_mov_b32_e32 v38, 0
	v_mov_b32_e32 v39, 0
	v_mov_b32_e32 v40, 0
	v_mov_b32_e32 v41, 0
	v_mov_b32_e32 v42, 0
	v_mov_b32_e32 v43, 0
	v_mov_b32_e32 v44, 0
	v_mov_b32_e32 v45, 0
	v_mov_b32_e32 v46, 0
	v_mov_b32_e32 v47, 0
	v_mov_b32_e32 v50, 0
	v_mov_b32_e32 v51, 0
	v_mov_b32_e32 v52, 0
	v_mov_b32_e32 v53, 0
	v_mov_b32_e32 v54, 0
	v_mov_b32_e32 v55, 0
	v_mov_b32_e32 v56, 0
	v_mov_b32_e32 v57, 0
	v_mov_b32_e32 v58, 0
	v_mov_b32_e32 v59, 0
	v_mov_b32_e32 v60, 0
	v_mov_b32_e32 v61, 0
	v_mov_b32_e32 v62, 0
	v_mov_b32_e32 v63, 0
	v_mov_b32_e32 v64, 0
	v_mov_b32_e32 v65, 0
	v_mov_b32_e32 v66, 0
	v_mov_b32_e32 v67, 0
	v_mov_b32_e32 v68, 0
	v_mov_b32_e32 v69, 0
	v_mov_b32_e32 v70, 0
	v_mov_b32_e32 v71, 0
	v_mov_b32_e32 v72, 0
	v_mov_b32_e32 v73, 0
	v_mov_b32_e32 v74, 0
	v_mov_b32_e32 v75, 0
	v_mov_b32_e32 v76, 0
	v_mov_b32_e32 v77, 0
	v_mov_b32_e32 v78, 0
	v_mov_b32_e32 v79, 0
	v_mov_b32_e32 v80, 0
	v_mov_b32_e32 v81, 0
	v_mov_b32_e32 v82, 0
	v_mov_b32_e32 v83, 0
	v_mov_b32_e32 v84, 0
	v_mov_b32_e32 v85, 0
	v_mov_b32_e32 v86, 0
	v_mov_b32_e32 v87, 0
	v_mov_b32_e32 v88, 0
	v_mov_b32_e32 v89, 0
	v_mov_b32_e32 v90, 0
	v_mov_b32_e32 v91, 0
	v_mov_b32_e32 v92, 0
	v_mov_b32_e32 v93, 0
	v_mov_b32_e32 v94, 0
	v_mov_b32_e32 v95, 0
	v_mov_b32_e32 v96, 0
	v_mov_b32_e32 v97, 0
	v_mov_b32_e32 v98, 0
	v_mov_b32_e32 v99, 0
	v_mov_b32_e32 v100, 0
	v_mov_b32_e32 v101, 0
	v_mov_b32_e32 v102, 0
	v_mov_b32_e32 v103, 0
	v_mov_b32_e32 v104, 0
	v_mov_b32_e32 v105, 0
	v_mov_b32_e32 v106, 0
	v_mov_b32_e32 v107, 0
	v_mov_b32_e32 v108, 0
	v_mov_b32_e32 v109, 0
	v_mov_b32_e32 v110, 0
	v_mov_b32_e32 v111, 0
	v_mov_b32_e32 v112, 0
	v_mov_b32_e32 v113, 0
	v_mov_b32_e32 v114, 0
	v_mov_b32_e32 v115, 0
	v_mov_b32_e32 v116, 0
	v_mov_b32_e32 v117, 0
	v_mov_b32_e32 v118, 0
	v_mov_b32_e32 v119, 0
	v_mov_b32_e32 v120, 0
	v_mov_b32_e32 v121, 0
	v_mov_b32_e32 v122, 0
	v_mov_b32_e32 v123, 0
	v_mov_b32_e32 v124, 0
	v_mov_b32_e32 v125, 0
	v_mov_b32_e32 v126, 0
	v_mov_b32_e32 v127, 0
	v_mov_b32_e32 v128, 0
	v_mov_b32_e32 v129, 0
	v_mov_b32_e32 v130, 0
	v_mov_b32_e32 v131, 0
	v_mov_b32_e32 v132, 0
	v_mov_b32_e32 v133, 0
	v_mov_b32_e32 v134, 0
	v_mov_b32_e32 v135, 0
	v_mov_b32_e32 v136, 0
	v_mov_b32_e32 v137, 0
	v_mov_b32_e32 v138, 0
	v_mov_b32_e32 v139, 0
	v_mov_b32_e32 v140, 0
	v_mov_b32_e32 v141, 0
	v_mov_b32_e32 v142, 0
	v_mov_b32_e32 v143, 0
	v_mov_b32_e32 v144, 0
	v_mov_b32_e32 v145, 0
	v_mov_b32_e32 v146, 0
	v_mov_b32_e32 v147, 0
	v_mov_b32_e32 v148, 0
	v_mov_b32_e32 v149, 0
	v_mov_b32_e32 v150, 0
	v_mov_b32_e32 v151, 0
	v_mov_b32_e32 v152, 0
	v_mov_b32_e32 v153, 0
	v_mov_b32_e32 v154, 0
	v_mov_b32_e32 v155, 0
	v_mov_b32_e32 v156, 0
	v_mov_b32_e32 v157, 0
	v_mov_b32_e32 v158, 0
	v_mov_b32_e32 v159, 0
	v_mov_b32_e32 v160, 0
	v_mov_b32_e32 v161, 0
	s_mov_b32 s100, 0
	s_branch .LBB0_135

.LBB0_137:
	s_ashr_i32 s61, s60, 31
	s_lshl_b64 s[12:13], s[60:61], 18
	s_add_u32 s64, s76, s12
	s_addc_u32 s65, s77, s13
	s_and_b64 s[12:13], s[38:39], exec
	s_cselect_b32 s7, s65, s5
	s_cselect_b32 s10, s64, s4
	s_ashr_i32 s63, s62, 31
	s_lshl_b64 s[12:13], s[62:63], 18
	s_add_u32 s66, s78, s12
	s_addc_u32 s67, s79, s13
	s_and_b64 s[12:13], s[38:39], exec
	s_cselect_b32 s12, s67, s1
	s_cselect_b32 s13, s66, s0
	s_add_u32 s70, s4, 0x20080
	s_addc_u32 s71, s5, 0
	s_add_u32 s4, s0, 0x100
	s_addc_u32 s5, s1, 0
	s_mov_b32 s14, -2
	s_add_u32 s0, s70, 0xfffe0080
	s_addc_u32 s1, s71, -1
	s_add_i32 s16, 0, 0x10000
	s_cmp_eq_u32 s14, 4
	s_cselect_b32 s73, s7, s1
	s_cselect_b32 s72, s10, s0
	s_cselect_b32 s1, s12, s5
	s_cselect_b32 s0, s13, s4
	s_add_i32 s18, 0, 0x14000
	v_add_u32_e32 v0, s16, v182
	v_add_u32_e32 v4, s18, v182
	ds_read_b128 v[24:27], v0
	ds_read_b128 v[28:31], v0 offset:1024
	ds_read_b128 v[16:19], v0 offset:2048
	ds_read_b128 v[20:23], v0 offset:3072
	ds_read_b128 v[8:11], v4
	ds_read_b128 v[12:15], v4 offset:1024
	ds_read_b128 v[0:3], v4 offset:2048
	ds_read_b128 v[4:7], v4 offset:3072
	v_lshl_add_u64 v[196:197], s[70:71], 0, v[170:171]
	s_add_i32 m0, s93, 0xc000
	ds_read_b128 v[174:177], v186
	ds_read_b128 v[178:181], v186 offset:1024
	ds_read_b128 v[188:191], v186 offset:2048
	ds_read_b128 v[192:195], v186 offset:3072
	ds_read_b128 v[206:209], v186 offset:4096
	ds_read_b128 v[210:213], v186 offset:5120
	ds_read_b128 v[214:217], v186 offset:6144
	ds_read_b128 v[218:221], v186 offset:7168
	global_load_lds_dwordx4 v[196:197], off
	v_lshl_add_u64 v[196:197], s[70:71], 0, v[172:173]
	s_add_i32 m0, s93, 0xe000
	s_nop 0
	global_load_lds_dwordx4 v[196:197], off
	s_waitcnt vmcnt(8)
	s_waitcnt lgkmcnt(0)
	s_barrier
	s_setprio 1
	s_waitcnt lgkmcnt(0)
	v_mfma_f32_16x16x128_f8f6f4 v[158:161], v[24:31], v[174:181], 0
	v_mfma_f32_16x16x128_f8f6f4 v[154:157], v[16:23], v[174:181], 0
	v_mfma_f32_16x16x128_f8f6f4 v[142:145], v[24:31], v[188:195], 0
	v_mfma_f32_16x16x128_f8f6f4 v[138:141], v[16:23], v[188:195], 0
	v_mfma_f32_16x16x128_f8f6f4 v[126:129], v[24:31], v[206:213], 0
	v_mfma_f32_16x16x128_f8f6f4 v[122:125], v[16:23], v[206:213], 0
	v_mfma_f32_16x16x128_f8f6f4 v[110:113], v[24:31], v[214:221], 0
	v_mfma_f32_16x16x128_f8f6f4 v[106:109], v[16:23], v[214:221], 0
	s_setprio 0
	s_setprio 1
	v_mfma_f32_16x16x128_f8f6f4 v[150:153], v[8:15], v[174:181], 0
	v_mfma_f32_16x16x128_f8f6f4 v[146:149], v[0:7], v[174:181], 0
	v_mfma_f32_16x16x128_f8f6f4 v[134:137], v[8:15], v[188:195], 0
	v_mfma_f32_16x16x128_f8f6f4 v[130:133], v[0:7], v[188:195], 0
	v_mfma_f32_16x16x128_f8f6f4 v[118:121], v[8:15], v[206:213], 0
	v_mfma_f32_16x16x128_f8f6f4 v[114:117], v[0:7], v[206:213], 0
	v_mfma_f32_16x16x128_f8f6f4 v[102:105], v[8:15], v[214:221], 0
	v_mfma_f32_16x16x128_f8f6f4 v[98:101], v[0:7], v[214:221], 0
	s_setprio 0
	s_barrier
	s_cmp_eq_u32 s100, 0
	s_cbranch_scc1 .Ldfs0
	global_store_dwordx4 v[222:223], v[198:201], off nt
.Ldfs0:
	s_add_i32 s16, s16, s80
	v_lshl_add_u64 v[174:175], s[0:1], 0, v[166:167]
	s_mov_b32 m0, s16
	ds_read_b128 v[188:191], v186 offset:16384
	ds_read_b128 v[192:195], v186 offset:17408
	ds_read_b128 v[206:209], v186 offset:18432
	ds_read_b128 v[210:213], v186 offset:19456
	ds_read_b128 v[214:217], v186 offset:20480
	ds_read_b128 v[218:221], v186 offset:21504
	ds_read_b128 v[240:243], v186 offset:22528
	ds_read_b128 v[244:247], v186 offset:23552
	global_load_lds_dwordx4 v[174:175], off
	s_add_i32 m0, s16, 0x2000
	s_add_u32 s20, s0, 0x8000
	v_lshl_add_u64 v[176:177], s[0:1], 0, v[162:163]
	s_addc_u32 s21, s1, 0
	s_add_i32 s16, s18, s80
	global_load_lds_dwordx4 v[176:177], off
	v_lshl_add_u64 v[178:179], s[20:21], 0, v[166:167]
	s_mov_b32 m0, s16
	v_lshl_add_u64 v[180:181], s[72:73], 0, v[164:165]
	global_load_lds_dwordx4 v[178:179], off
	v_lshl_add_u64 v[178:179], s[20:21], 0, v[162:163]
	s_add_i32 m0, s16, 0x2000
	s_nop 0
	global_load_lds_dwordx4 v[178:179], off
	v_lshl_add_u64 v[178:179], s[72:73], 0, v[168:169]
	s_mov_b32 m0, s93
	s_nop 0
	global_load_lds_dwordx4 v[178:179], off
	s_mov_b32 m0, s94
	s_nop 0
	global_load_lds_dwordx4 v[180:181], off
	s_cmp_eq_u32 s100, 0
	s_cbranch_scc1 .Ldfw0_n
	s_waitcnt vmcnt(9)
	s_branch .Ldfw0_j
.Ldfw0_n:
	s_waitcnt vmcnt(8)
.Ldfw0_j:
	s_waitcnt lgkmcnt(0)
	s_barrier
	s_setprio 1
	s_waitcnt lgkmcnt(0)
	v_mfma_f32_16x16x128_f8f6f4 v[94:97], v[24:31], v[188:195], 0
	v_mfma_f32_16x16x128_f8f6f4 v[90:93], v[16:23], v[188:195], 0
	v_mfma_f32_16x16x128_f8f6f4 v[70:73], v[24:31], v[206:213], 0
	v_mfma_f32_16x16x128_f8f6f4 v[66:69], v[16:23], v[206:213], 0
	v_mfma_f32_16x16x128_f8f6f4 v[44:47], v[24:31], v[214:221], 0
	v_mfma_f32_16x16x128_f8f6f4 v[40:43], v[16:23], v[214:221], 0
	v_mfma_f32_16x16x128_f8f6f4 v[36:39], v[24:31], v[240:247], 0
	v_mfma_f32_16x16x128_f8f6f4 v[32:35], v[16:23], v[240:247], 0
	s_setprio 0
	s_setprio 1
	v_mfma_f32_16x16x128_f8f6f4 v[86:89], v[8:15], v[188:195], 0
	v_mfma_f32_16x16x128_f8f6f4 v[82:85], v[0:7], v[188:195], 0
	v_mfma_f32_16x16x128_f8f6f4 v[62:65], v[8:15], v[206:213], 0
	v_mfma_f32_16x16x128_f8f6f4 v[50:53], v[0:7], v[206:213], 0
	v_mfma_f32_16x16x128_f8f6f4 v[78:81], v[8:15], v[214:221], 0
	v_mfma_f32_16x16x128_f8f6f4 v[74:77], v[0:7], v[214:221], 0
	v_mfma_f32_16x16x128_f8f6f4 v[58:61], v[8:15], v[240:247], 0
	v_mfma_f32_16x16x128_f8f6f4 v[54:57], v[0:7], v[240:247], 0
	s_setprio 0
	s_barrier
	s_cmp_eq_u32 s100, 0
	s_cbranch_scc1 .Ldfs1
	global_store_dwordx4 v[226:227], v[202:205], off nt
.Ldfs1:
	s_add_i32 s16, 0, 0x18000
	s_add_i32 s20, 0, 0x1c000
	v_add_u32_e32 v12, s16, v182
	v_add_u32_e32 v28, s20, v182
	ds_read_b128 v[0:3], v12
	ds_read_b128 v[4:7], v12 offset:1024
	ds_read_b128 v[8:11], v12 offset:2048
	ds_read_b128 v[12:15], v12 offset:3072
	ds_read_b128 v[16:19], v28
	ds_read_b128 v[20:23], v28 offset:1024
	ds_read_b128 v[24:27], v28 offset:2048
	ds_read_b128 v[28:31], v28 offset:3072
	s_add_u32 s18, s72, 0x20000
	s_addc_u32 s19, s73, 0
	s_mov_b32 m0, s95
	v_lshl_add_u64 v[196:197], s[18:19], 0, v[168:169]
	ds_read_b128 v[188:191], v186 offset:32768
	ds_read_b128 v[192:195], v186 offset:33792
	ds_read_b128 v[206:209], v186 offset:34816
	ds_read_b128 v[210:213], v186 offset:35840
	ds_read_b128 v[214:217], v186 offset:36864
	ds_read_b128 v[218:221], v186 offset:37888
	ds_read_b128 v[240:243], v186 offset:38912
	ds_read_b128 v[244:247], v186 offset:39936
	global_load_lds_dwordx4 v[196:197], off
	v_lshl_add_u64 v[196:197], s[18:19], 0, v[164:165]
	s_mov_b32 m0, s96
	s_nop 0
	global_load_lds_dwordx4 v[196:197], off
	s_cmp_eq_u32 s100, 0
	s_cbranch_scc1 .Ldfw1_n
	s_waitcnt vmcnt(10)
	s_branch .Ldfw1_j

.Ldfw1_j:
	s_waitcnt lgkmcnt(0)
	s_barrier
	s_setprio 1
	s_waitcnt lgkmcnt(0)
	v_mfma_f32_16x16x128_f8f6f4 v[158:161], v[0:7], v[188:195], v[158:161]
	v_mfma_f32_16x16x128_f8f6f4 v[154:157], v[8:15], v[188:195], v[154:157]
	v_mfma_f32_16x16x128_f8f6f4 v[142:145], v[0:7], v[206:213], v[142:145]
	v_mfma_f32_16x16x128_f8f6f4 v[138:141], v[8:15], v[206:213], v[138:141]
	v_mfma_f32_16x16x128_f8f6f4 v[126:129], v[0:7], v[214:221], v[126:129]
	v_mfma_f32_16x16x128_f8f6f4 v[122:125], v[8:15], v[214:221], v[122:125]
	v_mfma_f32_16x16x128_f8f6f4 v[110:113], v[0:7], v[240:247], v[110:113]
	v_mfma_f32_16x16x128_f8f6f4 v[106:109], v[8:15], v[240:247], v[106:109]
	s_setprio 0
	s_setprio 1
	v_mfma_f32_16x16x128_f8f6f4 v[150:153], v[16:23], v[188:195], v[150:153]
	v_mfma_f32_16x16x128_f8f6f4 v[146:149], v[24:31], v[188:195], v[146:149]
	v_mfma_f32_16x16x128_f8f6f4 v[134:137], v[16:23], v[206:213], v[134:137]
	v_mfma_f32_16x16x128_f8f6f4 v[130:133], v[24:31], v[206:213], v[130:133]
	v_mfma_f32_16x16x128_f8f6f4 v[118:121], v[16:23], v[214:221], v[118:121]
	v_mfma_f32_16x16x128_f8f6f4 v[114:117], v[24:31], v[214:221], v[114:117]
	v_mfma_f32_16x16x128_f8f6f4 v[102:105], v[16:23], v[240:247], v[102:105]
	v_mfma_f32_16x16x128_f8f6f4 v[98:101], v[24:31], v[240:247], v[98:101]
	s_setprio 0
	s_barrier
	s_cmp_eq_u32 s100, 0
	s_cbranch_scc1 .Ldfs2
	global_store_dwordx4 v[234:235], v[248:251], off nt
.Ldfs2:
	s_add_i32 s16, s16, s80
	v_lshl_add_u64 v[174:175], v[174:175], 0, s[88:89]
	s_mov_b32 m0, s16
	ds_read_b128 v[188:191], v186 offset:49152
	ds_read_b128 v[192:195], v186 offset:50176
	ds_read_b128 v[206:209], v186 offset:51200
	ds_read_b128 v[210:213], v186 offset:52224
	ds_read_b128 v[214:217], v186 offset:53248
	ds_read_b128 v[218:221], v186 offset:54272
	ds_read_b128 v[240:243], v186 offset:55296
	ds_read_b128 v[244:247], v186 offset:56320
	global_load_lds_dwordx4 v[174:175], off
	s_add_i32 m0, s16, 0x2000
	s_add_u32 s0, s0, 0x8080
	v_lshl_add_u64 v[174:175], v[176:177], 0, s[88:89]
	s_addc_u32 s1, s1, 0
	s_add_i32 s16, s20, s80
	global_load_lds_dwordx4 v[174:175], off
	v_lshl_add_u64 v[174:175], s[0:1], 0, v[166:167]
	s_mov_b32 m0, s16
	s_nop 0
	global_load_lds_dwordx4 v[174:175], off
	v_lshl_add_u64 v[174:175], s[0:1], 0, v[162:163]
	s_add_i32 m0, s16, 0x2000
	s_nop 0
	global_load_lds_dwordx4 v[174:175], off
	v_lshl_add_u64 v[174:175], v[178:179], 0, s[88:89]
	s_mov_b32 m0, s9
	s_nop 0
	global_load_lds_dwordx4 v[174:175], off
	v_lshl_add_u64 v[174:175], v[180:181], 0, s[88:89]
	s_mov_b32 m0, s97
	s_nop 0
	global_load_lds_dwordx4 v[174:175], off
	s_cmp_eq_u32 s100, 0
	s_cbranch_scc1 .Ldfw2_n
	s_waitcnt vmcnt(10)
	s_branch .Ldfw2_j

.Ldfw2_j:
	s_mov_b32 s100, 0
	s_waitcnt lgkmcnt(0)
	s_barrier
	s_setprio 1
	s_waitcnt lgkmcnt(0)
	v_mfma_f32_16x16x128_f8f6f4 v[94:97], v[0:7], v[188:195], v[94:97]
	v_mfma_f32_16x16x128_f8f6f4 v[90:93], v[8:15], v[188:195], v[90:93]
	v_mfma_f32_16x16x128_f8f6f4 v[70:73], v[0:7], v[206:213], v[70:73]
	v_mfma_f32_16x16x128_f8f6f4 v[66:69], v[8:15], v[206:213], v[66:69]
	v_mfma_f32_16x16x128_f8f6f4 v[44:47], v[0:7], v[214:221], v[44:47]
	v_mfma_f32_16x16x128_f8f6f4 v[40:43], v[8:15], v[214:221], v[40:43]
	v_mfma_f32_16x16x128_f8f6f4 v[36:39], v[0:7], v[240:247], v[36:39]
	v_mfma_f32_16x16x128_f8f6f4 v[32:35], v[8:15], v[240:247], v[32:35]
	s_setprio 0
	s_setprio 1
	v_mfma_f32_16x16x128_f8f6f4 v[86:89], v[16:23], v[188:195], v[86:89]
	v_mfma_f32_16x16x128_f8f6f4 v[82:85], v[24:31], v[188:195], v[82:85]
	v_mfma_f32_16x16x128_f8f6f4 v[62:65], v[16:23], v[206:213], v[62:65]
	v_mfma_f32_16x16x128_f8f6f4 v[50:53], v[24:31], v[206:213], v[50:53]
	v_mfma_f32_16x16x128_f8f6f4 v[78:81], v[16:23], v[214:221], v[78:81]
	v_mfma_f32_16x16x128_f8f6f4 v[74:77], v[24:31], v[214:221], v[74:77]
	v_mfma_f32_16x16x128_f8f6f4 v[58:61], v[16:23], v[240:247], v[58:61]
	v_mfma_f32_16x16x128_f8f6f4 v[54:57], v[24:31], v[240:247], v[54:57]
	s_setprio 0
	s_barrier
	s_add_i32 s14, s14, 2
	s_add_u32 s70, s70, 0x100
	s_addc_u32 s71, s71, 0
	s_add_u32 s4, s4, 0x100
	s_addc_u32 s5, s5, 0
	s_cmp_gt_u32 s14, 5

.LBB0_159:
	v_lshl_or_b32 v0, s6, 8, v185
	v_lshl_add_u32 v12, s68, 8, v183
	v_ashrrev_i32_e32 v1, 31, v0
	v_ashrrev_i32_e32 v2, 31, v12
	v_lshl_add_u64 v[0:1], v[0:1], 1, s[4:5]
	v_mul_lo_u32 v4, s0, v2
	v_mul_lo_u32 v5, s1, v12
	v_mad_u64_u32 v[2:3], s[4:5], s0, v12, 0
	v_add3_u32 v3, v3, v4, v5
	v_lshl_add_u64 v[10:11], v[2:3], 1, v[0:1]
	v_pk_mul_f32 v[2:3], v[160:161], s[70:71] op_sel_hi:[1,0]
	v_pk_mul_f32 v[4:5], v[158:159], s[70:71] op_sel_hi:[1,0]
	v_pk_mul_f32 v[6:7], v[156:157], s[70:71] op_sel_hi:[1,0]
	v_pk_mul_f32 v[8:9], v[154:155], s[70:71] op_sel_hi:[1,0]
	v_cvt_pk_bf16_f32 v13, v4, v5
	v_cvt_pk_bf16_f32 v14, v2, v3
	v_cvt_pk_bf16_f32 v15, v8, v9
	v_cvt_pk_bf16_f32 v16, v6, v7
	v_pk_mul_f32 v[2:3], v[152:153], s[70:71] op_sel_hi:[1,0]
	v_pk_mul_f32 v[4:5], v[150:151], s[70:71] op_sel_hi:[1,0]
	v_pk_mul_f32 v[6:7], v[148:149], s[70:71] op_sel_hi:[1,0]
	v_pk_mul_f32 v[8:9], v[146:147], s[70:71] op_sel_hi:[1,0]
	v_cvt_pk_bf16_f32 v17, v4, v5
	v_cvt_pk_bf16_f32 v18, v2, v3
	v_cvt_pk_bf16_f32 v8, v8, v9
	v_cvt_pk_bf16_f32 v6, v6, v7
	v_cndmask_b32_e64 v2, v16, v6, s[36:37]
	v_cndmask_b32_e64 v3, v14, v18, s[36:37]
	v_cndmask_b32_e64 v4, v15, v8, s[36:37]
	v_cndmask_b32_e64 v5, v13, v17, s[36:37]
	v_mov_b32_dpp v7, v3 quad_perm:[1,0,3,2] row_mask:0xf bank_mask:0xf bound_ctrl:1
	v_mov_b32_dpp v20, v4 quad_perm:[1,0,3,2] row_mask:0xf bank_mask:0xf bound_ctrl:1
	v_mov_b32_dpp v19, v5 quad_perm:[1,0,3,2] row_mask:0xf bank_mask:0xf bound_ctrl:1
	v_mov_b32_dpp v9, v2 quad_perm:[1,0,3,2] row_mask:0xf bank_mask:0xf bound_ctrl:1
	v_cndmask_b32_e64 v5, v9, v16, s[36:37]
	v_cndmask_b32_e64 v3, v7, v14, s[36:37]
	v_cndmask_b32_e64 v4, v20, v15, s[36:37]
	v_cndmask_b32_e64 v2, v19, v13, s[36:37]
	s_lshl_b64 s[68:69], s[0:1], 1
	v_cndmask_b32_e64 v9, v6, v9, s[36:37]
	v_cndmask_b32_e64 v7, v18, v7, s[36:37]
	v_cndmask_b32_e64 v8, v8, v20, s[36:37]
	v_cndmask_b32_e64 v6, v17, v19, s[36:37]
	global_store_dwordx4 v[10:11], v[2:5], off nt
	s_nop 1
	v_lshl_add_u64 v[2:3], v[10:11], 0, s[68:69]
	global_store_dwordx4 v[2:3], v[6:9], off nt
	v_add_u32_e32 v2, 16, v12
	v_ashrrev_i32_e32 v3, 31, v2
	v_mul_lo_u32 v4, s0, v3
	v_mul_lo_u32 v5, s1, v2
	v_mad_u64_u32 v[2:3], s[4:5], s0, v2, 0
	v_add3_u32 v3, v3, v4, v5
	v_lshl_add_u64 v[10:11], v[2:3], 1, v[0:1]
	v_pk_mul_f32 v[2:3], v[144:145], s[70:71] op_sel_hi:[1,0]
	v_pk_mul_f32 v[4:5], v[142:143], s[70:71] op_sel_hi:[1,0]
	v_pk_mul_f32 v[6:7], v[140:141], s[70:71] op_sel_hi:[1,0]
	v_pk_mul_f32 v[8:9], v[138:139], s[70:71] op_sel_hi:[1,0]
	v_cvt_pk_bf16_f32 v13, v4, v5
	v_cvt_pk_bf16_f32 v14, v2, v3
	v_cvt_pk_bf16_f32 v15, v8, v9
	v_cvt_pk_bf16_f32 v16, v6, v7
	v_pk_mul_f32 v[2:3], v[136:137], s[70:71] op_sel_hi:[1,0]
	v_pk_mul_f32 v[4:5], v[134:135], s[70:71] op_sel_hi:[1,0]
	v_pk_mul_f32 v[6:7], v[132:133], s[70:71] op_sel_hi:[1,0]
	v_pk_mul_f32 v[8:9], v[130:131], s[70:71] op_sel_hi:[1,0]
	v_cvt_pk_bf16_f32 v17, v4, v5
	v_cvt_pk_bf16_f32 v18, v2, v3
	v_cvt_pk_bf16_f32 v8, v8, v9
	v_cvt_pk_bf16_f32 v6, v6, v7
	v_cndmask_b32_e64 v2, v16, v6, s[36:37]
	v_cndmask_b32_e64 v3, v14, v18, s[36:37]
	v_cndmask_b32_e64 v4, v15, v8, s[36:37]
	v_cndmask_b32_e64 v5, v13, v17, s[36:37]
	v_mov_b32_dpp v7, v3 quad_perm:[1,0,3,2] row_mask:0xf bank_mask:0xf bound_ctrl:1
	v_mov_b32_dpp v20, v4 quad_perm:[1,0,3,2] row_mask:0xf bank_mask:0xf bound_ctrl:1
	v_mov_b32_dpp v19, v5 quad_perm:[1,0,3,2] row_mask:0xf bank_mask:0xf bound_ctrl:1
	v_mov_b32_dpp v9, v2 quad_perm:[1,0,3,2] row_mask:0xf bank_mask:0xf bound_ctrl:1
	v_cndmask_b32_e64 v5, v9, v16, s[36:37]
	v_cndmask_b32_e64 v3, v7, v14, s[36:37]
	v_cndmask_b32_e64 v4, v20, v15, s[36:37]
	v_cndmask_b32_e64 v2, v19, v13, s[36:37]
	v_cndmask_b32_e64 v9, v6, v9, s[36:37]
	v_cndmask_b32_e64 v7, v18, v7, s[36:37]
	v_cndmask_b32_e64 v8, v8, v20, s[36:37]
	v_cndmask_b32_e64 v6, v17, v19, s[36:37]
	global_store_dwordx4 v[10:11], v[2:5], off nt
	s_nop 1
	v_lshl_add_u64 v[2:3], v[10:11], 0, s[68:69]
	global_store_dwordx4 v[2:3], v[6:9], off nt
	v_add_u32_e32 v2, 32, v12
	v_ashrrev_i32_e32 v3, 31, v2
	v_mul_lo_u32 v4, s0, v3
	v_mul_lo_u32 v5, s1, v2
	v_mad_u64_u32 v[2:3], s[4:5], s0, v2, 0
	v_add3_u32 v3, v3, v4, v5
	v_lshl_add_u64 v[10:11], v[2:3], 1, v[0:1]
	v_pk_mul_f32 v[2:3], v[128:129], s[70:71] op_sel_hi:[1,0]
	v_pk_mul_f32 v[4:5], v[126:127], s[70:71] op_sel_hi:[1,0]
	v_pk_mul_f32 v[6:7], v[124:125], s[70:71] op_sel_hi:[1,0]
	v_pk_mul_f32 v[8:9], v[122:123], s[70:71] op_sel_hi:[1,0]
	v_cvt_pk_bf16_f32 v13, v4, v5
	v_cvt_pk_bf16_f32 v14, v2, v3
	v_cvt_pk_bf16_f32 v15, v8, v9
	v_cvt_pk_bf16_f32 v16, v6, v7
	v_pk_mul_f32 v[2:3], v[120:121], s[70:71] op_sel_hi:[1,0]
	v_pk_mul_f32 v[4:5], v[118:119], s[70:71] op_sel_hi:[1,0]
	v_pk_mul_f32 v[6:7], v[116:117], s[70:71] op_sel_hi:[1,0]
	v_pk_mul_f32 v[8:9], v[114:115], s[70:71] op_sel_hi:[1,0]
	v_cvt_pk_bf16_f32 v17, v4, v5
	v_cvt_pk_bf16_f32 v18, v2, v3
	v_cvt_pk_bf16_f32 v8, v8, v9
	v_cvt_pk_bf16_f32 v6, v6, v7
	v_cndmask_b32_e64 v2, v16, v6, s[36:37]
	v_cndmask_b32_e64 v3, v14, v18, s[36:37]
	v_cndmask_b32_e64 v4, v15, v8, s[36:37]
	v_cndmask_b32_e64 v5, v13, v17, s[36:37]
	v_mov_b32_dpp v7, v3 quad_perm:[1,0,3,2] row_mask:0xf bank_mask:0xf bound_ctrl:1
	v_mov_b32_dpp v20, v4 quad_perm:[1,0,3,2] row_mask:0xf bank_mask:0xf bound_ctrl:1
	v_mov_b32_dpp v19, v5 quad_perm:[1,0,3,2] row_mask:0xf bank_mask:0xf bound_ctrl:1
	v_mov_b32_dpp v9, v2 quad_perm:[1,0,3,2] row_mask:0xf bank_mask:0xf bound_ctrl:1
	v_cndmask_b32_e64 v5, v9, v16, s[36:37]
	v_cndmask_b32_e64 v3, v7, v14, s[36:37]
	v_cndmask_b32_e64 v4, v20, v15, s[36:37]
	v_cndmask_b32_e64 v2, v19, v13, s[36:37]
	v_cndmask_b32_e64 v9, v6, v9, s[36:37]
	v_cndmask_b32_e64 v7, v18, v7, s[36:37]
	v_cndmask_b32_e64 v8, v8, v20, s[36:37]
	v_cndmask_b32_e64 v6, v17, v19, s[36:37]
	global_store_dwordx4 v[10:11], v[2:5], off nt
	s_nop 1
	v_lshl_add_u64 v[2:3], v[10:11], 0, s[68:69]
	global_store_dwordx4 v[2:3], v[6:9], off nt
	v_add_u32_e32 v2, 48, v12
	v_ashrrev_i32_e32 v3, 31, v2
	v_mul_lo_u32 v4, s0, v3
	v_mul_lo_u32 v5, s1, v2
	v_mad_u64_u32 v[2:3], s[4:5], s0, v2, 0
	v_add3_u32 v3, v3, v4, v5
	v_lshl_add_u64 v[10:11], v[2:3], 1, v[0:1]
	v_pk_mul_f32 v[2:3], v[112:113], s[70:71] op_sel_hi:[1,0]
	v_pk_mul_f32 v[4:5], v[110:111], s[70:71] op_sel_hi:[1,0]
	v_pk_mul_f32 v[6:7], v[108:109], s[70:71] op_sel_hi:[1,0]
	v_pk_mul_f32 v[8:9], v[106:107], s[70:71] op_sel_hi:[1,0]
	v_cvt_pk_bf16_f32 v13, v4, v5
	v_cvt_pk_bf16_f32 v14, v2, v3
	v_cvt_pk_bf16_f32 v15, v8, v9
	v_cvt_pk_bf16_f32 v16, v6, v7
	v_pk_mul_f32 v[2:3], v[104:105], s[70:71] op_sel_hi:[1,0]
	v_pk_mul_f32 v[4:5], v[102:103], s[70:71] op_sel_hi:[1,0]
	v_pk_mul_f32 v[6:7], v[100:101], s[70:71] op_sel_hi:[1,0]
	v_pk_mul_f32 v[8:9], v[98:99], s[70:71] op_sel_hi:[1,0]
	v_cvt_pk_bf16_f32 v17, v4, v5
	v_cvt_pk_bf16_f32 v18, v2, v3
	v_cvt_pk_bf16_f32 v8, v8, v9
	v_cvt_pk_bf16_f32 v6, v6, v7
	v_cndmask_b32_e64 v2, v16, v6, s[36:37]
	v_cndmask_b32_e64 v3, v14, v18, s[36:37]
	v_cndmask_b32_e64 v4, v15, v8, s[36:37]
	v_cndmask_b32_e64 v5, v13, v17, s[36:37]
	v_mov_b32_dpp v7, v3 quad_perm:[1,0,3,2] row_mask:0xf bank_mask:0xf bound_ctrl:1
	v_mov_b32_dpp v20, v4 quad_perm:[1,0,3,2] row_mask:0xf bank_mask:0xf bound_ctrl:1
	v_mov_b32_dpp v19, v5 quad_perm:[1,0,3,2] row_mask:0xf bank_mask:0xf bound_ctrl:1
	v_mov_b32_dpp v9, v2 quad_perm:[1,0,3,2] row_mask:0xf bank_mask:0xf bound_ctrl:1
	v_cndmask_b32_e64 v5, v9, v16, s[36:37]
	v_cndmask_b32_e64 v3, v7, v14, s[36:37]
	v_cndmask_b32_e64 v4, v20, v15, s[36:37]
	v_cndmask_b32_e64 v2, v19, v13, s[36:37]
	v_cndmask_b32_e64 v9, v6, v9, s[36:37]
	v_cndmask_b32_e64 v7, v18, v7, s[36:37]
	v_cndmask_b32_e64 v8, v8, v20, s[36:37]
	v_cndmask_b32_e64 v6, v17, v19, s[36:37]
	global_store_dwordx4 v[10:11], v[2:5], off nt
	s_nop 1
	v_lshl_add_u64 v[2:3], v[10:11], 0, s[68:69]
	global_store_dwordx4 v[2:3], v[6:9], off nt
	v_add_u32_e32 v2, 0x80, v12
	v_ashrrev_i32_e32 v3, 31, v2
	v_mul_lo_u32 v4, s0, v3
	v_mul_lo_u32 v5, s1, v2
	v_mad_u64_u32 v[2:3], s[4:5], s0, v2, 0
	v_add3_u32 v3, v3, v4, v5
	v_lshl_add_u64 v[10:11], v[2:3], 1, v[0:1]
	v_pk_mul_f32 v[2:3], v[96:97], s[70:71] op_sel_hi:[1,0]
	v_pk_mul_f32 v[4:5], v[94:95], s[70:71] op_sel_hi:[1,0]
	v_pk_mul_f32 v[6:7], v[92:93], s[70:71] op_sel_hi:[1,0]
	v_pk_mul_f32 v[8:9], v[90:91], s[70:71] op_sel_hi:[1,0]
	v_cvt_pk_bf16_f32 v13, v4, v5
	v_cvt_pk_bf16_f32 v14, v2, v3
	v_cvt_pk_bf16_f32 v15, v8, v9
	v_cvt_pk_bf16_f32 v16, v6, v7
	v_pk_mul_f32 v[2:3], v[88:89], s[70:71] op_sel_hi:[1,0]
	v_pk_mul_f32 v[4:5], v[86:87], s[70:71] op_sel_hi:[1,0]
	v_pk_mul_f32 v[6:7], v[84:85], s[70:71] op_sel_hi:[1,0]
	v_pk_mul_f32 v[8:9], v[82:83], s[70:71] op_sel_hi:[1,0]
	v_cvt_pk_bf16_f32 v17, v4, v5
	v_cvt_pk_bf16_f32 v18, v2, v3
	v_cvt_pk_bf16_f32 v8, v8, v9
	v_cvt_pk_bf16_f32 v6, v6, v7
	v_cndmask_b32_e64 v2, v16, v6, s[36:37]
	v_cndmask_b32_e64 v3, v14, v18, s[36:37]
	v_cndmask_b32_e64 v4, v15, v8, s[36:37]
	v_cndmask_b32_e64 v5, v13, v17, s[36:37]
	v_mov_b32_dpp v7, v3 quad_perm:[1,0,3,2] row_mask:0xf bank_mask:0xf bound_ctrl:1
	v_mov_b32_dpp v20, v4 quad_perm:[1,0,3,2] row_mask:0xf bank_mask:0xf bound_ctrl:1
	v_mov_b32_dpp v19, v5 quad_perm:[1,0,3,2] row_mask:0xf bank_mask:0xf bound_ctrl:1
	v_mov_b32_dpp v9, v2 quad_perm:[1,0,3,2] row_mask:0xf bank_mask:0xf bound_ctrl:1
	v_cndmask_b32_e64 v5, v9, v16, s[36:37]
	v_cndmask_b32_e64 v3, v7, v14, s[36:37]
	v_cndmask_b32_e64 v4, v20, v15, s[36:37]
	v_cndmask_b32_e64 v2, v19, v13, s[36:37]
	v_cndmask_b32_e64 v9, v6, v9, s[36:37]
	v_cndmask_b32_e64 v7, v18, v7, s[36:37]
	v_cndmask_b32_e64 v8, v8, v20, s[36:37]
	v_cndmask_b32_e64 v6, v17, v19, s[36:37]
	global_store_dwordx4 v[10:11], v[2:5], off nt
	s_nop 1
	v_lshl_add_u64 v[2:3], v[10:11], 0, s[68:69]
	global_store_dwordx4 v[2:3], v[6:9], off nt
	v_add_u32_e32 v2, 0x90, v12
	v_ashrrev_i32_e32 v3, 31, v2
	v_mul_lo_u32 v4, s0, v3
	v_mul_lo_u32 v5, s1, v2
	v_mad_u64_u32 v[2:3], s[4:5], s0, v2, 0
	v_add3_u32 v3, v3, v4, v5
	v_lshl_add_u64 v[10:11], v[2:3], 1, v[0:1]
	v_pk_mul_f32 v[2:3], v[72:73], s[70:71] op_sel_hi:[1,0]
	v_pk_mul_f32 v[4:5], v[70:71], s[70:71] op_sel_hi:[1,0]
	v_pk_mul_f32 v[6:7], v[68:69], s[70:71] op_sel_hi:[1,0]
	v_pk_mul_f32 v[8:9], v[66:67], s[70:71] op_sel_hi:[1,0]
	v_cvt_pk_bf16_f32 v13, v4, v5
	v_cvt_pk_bf16_f32 v14, v2, v3
	v_cvt_pk_bf16_f32 v15, v8, v9
	v_cvt_pk_bf16_f32 v16, v6, v7
	v_pk_mul_f32 v[2:3], v[64:65], s[70:71] op_sel_hi:[1,0]
	v_pk_mul_f32 v[4:5], v[62:63], s[70:71] op_sel_hi:[1,0]
	v_pk_mul_f32 v[6:7], v[52:53], s[70:71] op_sel_hi:[1,0]
	v_pk_mul_f32 v[8:9], v[50:51], s[70:71] op_sel_hi:[1,0]
	v_cvt_pk_bf16_f32 v17, v4, v5
	v_cvt_pk_bf16_f32 v18, v2, v3
	v_cvt_pk_bf16_f32 v8, v8, v9
	v_cvt_pk_bf16_f32 v6, v6, v7
	v_cndmask_b32_e64 v2, v16, v6, s[36:37]
	v_cndmask_b32_e64 v3, v14, v18, s[36:37]
	v_cndmask_b32_e64 v4, v15, v8, s[36:37]
	v_cndmask_b32_e64 v5, v13, v17, s[36:37]
	v_mov_b32_dpp v7, v3 quad_perm:[1,0,3,2] row_mask:0xf bank_mask:0xf bound_ctrl:1
	v_mov_b32_dpp v20, v4 quad_perm:[1,0,3,2] row_mask:0xf bank_mask:0xf bound_ctrl:1
	v_mov_b32_dpp v19, v5 quad_perm:[1,0,3,2] row_mask:0xf bank_mask:0xf bound_ctrl:1
	v_mov_b32_dpp v9, v2 quad_perm:[1,0,3,2] row_mask:0xf bank_mask:0xf bound_ctrl:1
	v_cndmask_b32_e64 v5, v9, v16, s[36:37]
	v_cndmask_b32_e64 v3, v7, v14, s[36:37]
	v_cndmask_b32_e64 v4, v20, v15, s[36:37]
	v_cndmask_b32_e64 v2, v19, v13, s[36:37]
	v_cndmask_b32_e64 v9, v6, v9, s[36:37]
	v_cndmask_b32_e64 v7, v18, v7, s[36:37]
	v_cndmask_b32_e64 v8, v8, v20, s[36:37]
	v_cndmask_b32_e64 v6, v17, v19, s[36:37]
	global_store_dwordx4 v[10:11], v[2:5], off nt
	s_nop 1
	v_lshl_add_u64 v[2:3], v[10:11], 0, s[68:69]
	global_store_dwordx4 v[2:3], v[6:9], off nt
	v_add_u32_e32 v2, 0xa0, v12
	v_ashrrev_i32_e32 v3, 31, v2
	v_mul_lo_u32 v4, s0, v3
	v_mul_lo_u32 v5, s1, v2
	v_mad_u64_u32 v[2:3], s[4:5], s0, v2, 0
	v_add3_u32 v3, v3, v4, v5
	v_lshl_add_u64 v[10:11], v[2:3], 1, v[0:1]
	v_pk_mul_f32 v[2:3], v[46:47], s[70:71] op_sel_hi:[1,0]
	v_pk_mul_f32 v[4:5], v[44:45], s[70:71] op_sel_hi:[1,0]
	v_pk_mul_f32 v[6:7], v[42:43], s[70:71] op_sel_hi:[1,0]
	v_pk_mul_f32 v[8:9], v[40:41], s[70:71] op_sel_hi:[1,0]
	v_cvt_pk_bf16_f32 v13, v4, v5
	v_cvt_pk_bf16_f32 v14, v2, v3
	v_cvt_pk_bf16_f32 v15, v8, v9
	v_cvt_pk_bf16_f32 v16, v6, v7
	v_pk_mul_f32 v[2:3], v[80:81], s[70:71] op_sel_hi:[1,0]
	v_pk_mul_f32 v[4:5], v[78:79], s[70:71] op_sel_hi:[1,0]
	v_pk_mul_f32 v[6:7], v[76:77], s[70:71] op_sel_hi:[1,0]
	v_pk_mul_f32 v[8:9], v[74:75], s[70:71] op_sel_hi:[1,0]
	v_cvt_pk_bf16_f32 v17, v4, v5
	v_cvt_pk_bf16_f32 v18, v2, v3
	v_cvt_pk_bf16_f32 v8, v8, v9
	v_cvt_pk_bf16_f32 v6, v6, v7
	v_cndmask_b32_e64 v2, v16, v6, s[36:37]
	v_cndmask_b32_e64 v3, v14, v18, s[36:37]
	v_cndmask_b32_e64 v4, v15, v8, s[36:37]
	v_cndmask_b32_e64 v5, v13, v17, s[36:37]
	v_mov_b32_dpp v7, v3 quad_perm:[1,0,3,2] row_mask:0xf bank_mask:0xf bound_ctrl:1
	v_mov_b32_dpp v20, v4 quad_perm:[1,0,3,2] row_mask:0xf bank_mask:0xf bound_ctrl:1
	v_mov_b32_dpp v19, v5 quad_perm:[1,0,3,2] row_mask:0xf bank_mask:0xf bound_ctrl:1
	v_mov_b32_dpp v9, v2 quad_perm:[1,0,3,2] row_mask:0xf bank_mask:0xf bound_ctrl:1
	v_cndmask_b32_e64 v5, v9, v16, s[36:37]
	v_cndmask_b32_e64 v3, v7, v14, s[36:37]
	v_cndmask_b32_e64 v4, v20, v15, s[36:37]
	v_cndmask_b32_e64 v2, v19, v13, s[36:37]
	v_cndmask_b32_e64 v9, v6, v9, s[36:37]
	v_cndmask_b32_e64 v7, v18, v7, s[36:37]
	v_cndmask_b32_e64 v8, v8, v20, s[36:37]
	v_cndmask_b32_e64 v6, v17, v19, s[36:37]
	global_store_dwordx4 v[10:11], v[2:5], off nt
	s_nop 1
	v_lshl_add_u64 v[222:223], v[10:11], 0, s[68:69]
	v_mov_b32_e32 v198, v6
	v_mov_b32_e32 v199, v7
	v_mov_b32_e32 v200, v8
	v_mov_b32_e32 v201, v9
	v_add_u32_e32 v2, 0xb0, v12
	v_ashrrev_i32_e32 v3, 31, v2
	v_mul_lo_u32 v4, s0, v3
	v_mul_lo_u32 v5, s1, v2
	v_mad_u64_u32 v[2:3], s[0:1], s0, v2, 0
	v_add3_u32 v3, v3, v4, v5
	v_lshl_add_u64 v[8:9], v[2:3], 1, v[0:1]
	v_pk_mul_f32 v[0:1], v[38:39], s[70:71] op_sel_hi:[1,0]
	v_pk_mul_f32 v[2:3], v[36:37], s[70:71] op_sel_hi:[1,0]
	v_pk_mul_f32 v[4:5], v[34:35], s[70:71] op_sel_hi:[1,0]
	v_pk_mul_f32 v[6:7], v[32:33], s[70:71] op_sel_hi:[1,0]
	v_cvt_pk_bf16_f32 v10, v2, v3
	v_cvt_pk_bf16_f32 v11, v0, v1
	v_cvt_pk_bf16_f32 v12, v6, v7
	v_cvt_pk_bf16_f32 v13, v4, v5
	v_pk_mul_f32 v[0:1], v[60:61], s[70:71] op_sel_hi:[1,0]
	v_pk_mul_f32 v[2:3], v[58:59], s[70:71] op_sel_hi:[1,0]
	v_pk_mul_f32 v[4:5], v[56:57], s[70:71] op_sel_hi:[1,0]
	v_pk_mul_f32 v[6:7], v[54:55], s[70:71] op_sel_hi:[1,0]
	v_cvt_pk_bf16_f32 v14, v2, v3
	v_cvt_pk_bf16_f32 v15, v0, v1
	v_cvt_pk_bf16_f32 v6, v6, v7
	v_cvt_pk_bf16_f32 v4, v4, v5
	v_cndmask_b32_e64 v0, v13, v4, s[36:37]
	v_cndmask_b32_e64 v1, v11, v15, s[36:37]
	v_cndmask_b32_e64 v2, v12, v6, s[36:37]
	v_cndmask_b32_e64 v3, v10, v14, s[36:37]
	v_mov_b32_dpp v5, v1 quad_perm:[1,0,3,2] row_mask:0xf bank_mask:0xf bound_ctrl:1
	v_mov_b32_dpp v17, v2 quad_perm:[1,0,3,2] row_mask:0xf bank_mask:0xf bound_ctrl:1
	v_mov_b32_dpp v16, v3 quad_perm:[1,0,3,2] row_mask:0xf bank_mask:0xf bound_ctrl:1
	v_mov_b32_dpp v7, v0 quad_perm:[1,0,3,2] row_mask:0xf bank_mask:0xf bound_ctrl:1
	v_cndmask_b32_e64 v3, v7, v13, s[36:37]
	v_cndmask_b32_e64 v1, v5, v11, s[36:37]
	v_cndmask_b32_e64 v2, v17, v12, s[36:37]
	v_cndmask_b32_e64 v0, v16, v10, s[36:37]
	v_cndmask_b32_e64 v7, v4, v7, s[36:37]
	v_cndmask_b32_e64 v5, v15, v5, s[36:37]
	v_cndmask_b32_e64 v6, v6, v17, s[36:37]
	v_cndmask_b32_e64 v4, v14, v16, s[36:37]
	v_mov_b32_e32 v202, v0
	v_mov_b32_e32 v203, v1
	v_mov_b32_e32 v204, v2
	v_mov_b32_e32 v205, v3
	v_mov_b32_e32 v226, v8
	v_mov_b32_e32 v227, v9
	s_nop 1
	v_lshl_add_u64 v[234:235], v[8:9], 0, s[68:69]
	v_mov_b32_e32 v248, v4
	v_mov_b32_e32 v249, v5
	v_mov_b32_e32 v250, v6
	v_mov_b32_e32 v251, v7
	s_mov_b32 s100, 1
	s_andn2_b64 vcc, exec, s[38:39]
	s_mov_b64 s[0:1], -1
	s_cbranch_vccnz .LBB0_134

.LBB0_163:
	s_cmp_eq_u32 s100, 0
	s_cbranch_scc1 .Ldf_fl
	global_store_dwordx4 v[222:223], v[198:201], off nt
	global_store_dwordx4 v[226:227], v[202:205], off nt
	global_store_dwordx4 v[234:235], v[248:251], off nt
	s_mov_b32 s100, 0

	.amdhsa_kernel _Z6mk_fwd4Args
		.amdhsa_group_segment_fixed_size 0
		.amdhsa_private_segment_fixed_size 0
		.amdhsa_kernarg_size 384
		.amdhsa_user_sgpr_count 2
		.amdhsa_user_sgpr_dispatch_ptr 0
		.amdhsa_user_sgpr_queue_ptr 0
		.amdhsa_user_sgpr_kernarg_segment_ptr 1
		.amdhsa_user_sgpr_dispatch_id 0
		.amdhsa_user_sgpr_kernarg_preload_length 0
		.amdhsa_user_sgpr_kernarg_preload_offset 0
		.amdhsa_user_sgpr_private_segment_size 0
		.amdhsa_uses_dynamic_stack 0
		.amdhsa_enable_private_segment 0
		.amdhsa_system_sgpr_workgroup_id_x 1
		.amdhsa_system_sgpr_workgroup_id_y 0
		.amdhsa_system_sgpr_workgroup_id_z 0
		.amdhsa_system_sgpr_workgroup_info 0
		.amdhsa_system_vgpr_workitem_id 0
		.amdhsa_next_free_vgpr 256
		.amdhsa_next_free_sgpr 102
		.amdhsa_accum_offset 256
		.amdhsa_reserve_vcc 1
		.amdhsa_float_round_mode_32 0
		.amdhsa_float_round_mode_16_64 0
		.amdhsa_float_denorm_mode_32 3
		.amdhsa_float_denorm_mode_16_64 3
		.amdhsa_dx10_clamp 1
		.amdhsa_ieee_mode 1
		.amdhsa_fp16_overflow 0
		.amdhsa_tg_split 0
		.amdhsa_exception_fp_ieee_invalid_op 0
		.amdhsa_exception_fp_denorm_src 0
		.amdhsa_exception_fp_ieee_div_zero 0
		.amdhsa_exception_fp_ieee_overflow 0
		.amdhsa_exception_fp_ieee_underflow 0
		.amdhsa_exception_fp_ieee_inexact 0
		.amdhsa_exception_int_div_zero 0
	.end_amdhsa_kernel

amdhsa.kernels:
  - .agpr_count:     0
    .args:
      - .offset:         0
        .size:           128
        .value_kind:     by_value
      - .offset:         128
        .size:           4
        .value_kind:     hidden_block_count_x
      - .offset:         132
        .size:           4
        .value_kind:     hidden_block_count_y
      - .offset:         136
        .size:           4
        .value_kind:     hidden_block_count_z
      - .offset:         140
        .size:           2
        .value_kind:     hidden_group_size_x
      - .offset:         142
        .size:           2
        .value_kind:     hidden_group_size_y
      - .offset:         144
        .size:           2
        .value_kind:     hidden_group_size_z
      - .offset:         146
        .size:           2
        .value_kind:     hidden_remainder_x
      - .offset:         148
        .size:           2
        .value_kind:     hidden_remainder_y
      - .offset:         150
        .size:           2
        .value_kind:     hidden_remainder_z
      - .offset:         168
        .size:           8
        .value_kind:     hidden_global_offset_x
      - .offset:         176
        .size:           8
        .value_kind:     hidden_global_offset_y
      - .offset:         184
        .size:           8
        .value_kind:     hidden_global_offset_z
      - .offset:         192
        .size:           2
        .value_kind:     hidden_grid_dims
      - .offset:         248
        .size:           4
        .value_kind:     hidden_dynamic_lds_size
    .group_segment_fixed_size: 0
    .kernarg_segment_align: 8
    .kernarg_segment_size: 384
    .language:       OpenCL C
    .language_version:
      - 2
      - 0
    .max_flat_workgroup_size: 512
    .name:           _Z6mk_fwd4Args
    .private_segment_fixed_size: 0
    .sgpr_count:     108
    .sgpr_spill_count: 165
    .symbol:         _Z6mk_fwd4Args.kd
    .uniform_work_group_size: 1
    .uses_dynamic_stack: false
    .vgpr_count:     256
    .vgpr_spill_count: 0
    .wavefront_size: 64
